# dynamic chunks + e2f in gather shadow + L1-warming E-row prefetches (screening argmin rows, slow-path candidates)
# baseline (speedup 1.0000x reference)
.Lfront_nocursor:
	s_waitcnt lgkmcnt(0)
	s_barrier
	s_mov_b64 exec, s[36:37]
	ds_add_rtn_u32 v106, v74, v143 offset:64
	s_mov_b64 exec, s[38:39]
	ds_add_rtn_u32 v107, v75, v143 offset:64
	s_mov_b64 exec, s[40:41]
	ds_add_rtn_u32 v108, v76, v143 offset:64
	s_mov_b64 exec, s[42:43]
	ds_add_rtn_u32 v109, v77, v143 offset:64
	s_mov_b64 exec, s[44:45]
	ds_add_rtn_u32 v110, v78, v143 offset:64
	s_mov_b64 exec, s[46:47]
	ds_add_rtn_u32 v111, v79, v143 offset:64
	s_mov_b64 exec, s[48:49]
	ds_add_rtn_u32 v112, v80, v143 offset:64
	s_mov_b64 exec, s[50:51]
	ds_add_rtn_u32 v113, v81, v143 offset:64
	s_mov_b64 exec, s[52:53]
	ds_add_rtn_u32 v114, v82, v143 offset:64
	s_mov_b64 exec, s[54:55]
	ds_add_rtn_u32 v115, v83, v143 offset:64
	s_mov_b64 exec, s[56:57]
	ds_add_rtn_u32 v116, v84, v143 offset:64
	s_mov_b64 exec, s[58:59]
	ds_add_rtn_u32 v117, v85, v143 offset:64
	s_mov_b64 exec, s[60:61]
	ds_add_rtn_u32 v118, v86, v143 offset:64
	s_mov_b64 exec, s[62:63]
	ds_add_rtn_u32 v119, v87, v143 offset:64
	s_mov_b64 exec, s[64:65]
	ds_add_rtn_u32 v120, v88, v143 offset:64
	s_mov_b64 exec, s[66:67]
	ds_add_rtn_u32 v121, v89, v143 offset:64
	s_mov_b64 exec, s[68:69]
	ds_add_rtn_u32 v122, v90, v143 offset:64
	s_mov_b64 exec, s[70:71]
	ds_add_rtn_u32 v123, v91, v143 offset:64
	s_mov_b64 exec, s[72:73]
	ds_add_rtn_u32 v124, v92, v143 offset:64
	s_mov_b64 exec, s[74:75]
	ds_add_rtn_u32 v125, v93, v143 offset:64
	s_mov_b64 exec, s[76:77]
	ds_add_rtn_u32 v126, v94, v143 offset:64
	s_mov_b64 exec, s[78:79]
	ds_add_rtn_u32 v127, v95, v143 offset:64
	s_mov_b64 exec, s[80:81]
	ds_add_rtn_u32 v128, v96, v143 offset:64
	s_mov_b64 exec, s[82:83]
	ds_add_rtn_u32 v129, v97, v143 offset:64
	s_mov_b64 exec, s[84:85]
	ds_add_rtn_u32 v130, v98, v143 offset:64
	s_mov_b64 exec, s[86:87]
	ds_add_rtn_u32 v131, v99, v143 offset:64
	s_mov_b64 exec, s[88:89]
	ds_add_rtn_u32 v132, v100, v143 offset:64
	s_mov_b64 exec, s[90:91]
	ds_add_rtn_u32 v133, v101, v143 offset:64
	s_mov_b64 exec, s[92:93]
	ds_add_rtn_u32 v134, v102, v143 offset:64
	s_mov_b64 exec, s[94:95]
	ds_add_rtn_u32 v135, v103, v143 offset:64
	s_mov_b64 exec, s[96:97]
	ds_add_rtn_u32 v136, v104, v143 offset:64
	s_mov_b64 exec, s[98:99]
	ds_add_rtn_u32 v137, v105, v143 offset:64
	s_mov_b64 exec, -1
	v_add_u32_e32 v146, 0x0, v145
	v_and_or_b32 v146, v74, 60, v146
	s_waitcnt lgkmcnt(0)
	s_mov_b64 exec, s[36:37]
	ds_write_b32 v106, v146
	s_mov_b64 exec, -1
	v_add_u32_e32 v147, 0x40, v145
	v_and_or_b32 v147, v75, 60, v147
	s_mov_b64 exec, s[38:39]
	ds_write_b32 v107, v147
	s_mov_b64 exec, -1
	v_add_u32_e32 v146, 0x80, v145
	v_and_or_b32 v146, v76, 60, v146
	s_mov_b64 exec, s[40:41]
	ds_write_b32 v108, v146
	s_mov_b64 exec, -1
	v_add_u32_e32 v147, 0xc0, v145
	v_and_or_b32 v147, v77, 60, v147
	s_mov_b64 exec, s[42:43]
	ds_write_b32 v109, v147
	s_mov_b64 exec, -1
	v_add_u32_e32 v146, 0x10000, v145
	v_and_or_b32 v146, v78, 60, v146
	s_mov_b64 exec, s[44:45]
	ds_write_b32 v110, v146
	s_mov_b64 exec, -1
	v_add_u32_e32 v147, 0x10040, v145
	v_and_or_b32 v147, v79, 60, v147
	s_mov_b64 exec, s[46:47]
	ds_write_b32 v111, v147
	s_mov_b64 exec, -1
	v_add_u32_e32 v146, 0x10080, v145
	v_and_or_b32 v146, v80, 60, v146
	s_mov_b64 exec, s[48:49]
	ds_write_b32 v112, v146
	s_mov_b64 exec, -1
	v_add_u32_e32 v147, 0x100c0, v145
	v_and_or_b32 v147, v81, 60, v147
	s_mov_b64 exec, s[50:51]
	ds_write_b32 v113, v147
	s_mov_b64 exec, -1
	v_add_u32_e32 v146, 0x20000, v145
	v_and_or_b32 v146, v82, 60, v146
	s_mov_b64 exec, s[52:53]
	ds_write_b32 v114, v146
	s_mov_b64 exec, -1
	v_add_u32_e32 v147, 0x20040, v145
	v_and_or_b32 v147, v83, 60, v147
	s_mov_b64 exec, s[54:55]
	ds_write_b32 v115, v147
	s_mov_b64 exec, -1
	v_add_u32_e32 v146, 0x20080, v145
	v_and_or_b32 v146, v84, 60, v146
	s_mov_b64 exec, s[56:57]
	ds_write_b32 v116, v146
	s_mov_b64 exec, -1
	v_add_u32_e32 v147, 0x200c0, v145
	v_and_or_b32 v147, v85, 60, v147
	s_mov_b64 exec, s[58:59]
	ds_write_b32 v117, v147
	s_mov_b64 exec, -1
	v_add_u32_e32 v146, 0x30000, v145
	v_and_or_b32 v146, v86, 60, v146
	s_mov_b64 exec, s[60:61]
	ds_write_b32 v118, v146
	s_mov_b64 exec, -1
	v_add_u32_e32 v147, 0x30040, v145
	v_and_or_b32 v147, v87, 60, v147
	s_mov_b64 exec, s[62:63]
	ds_write_b32 v119, v147
	s_mov_b64 exec, -1
	v_add_u32_e32 v146, 0x30080, v145
	v_and_or_b32 v146, v88, 60, v146
	s_mov_b64 exec, s[64:65]
	ds_write_b32 v120, v146
	s_mov_b64 exec, -1
	v_add_u32_e32 v147, 0x300c0, v145
	v_and_or_b32 v147, v89, 60, v147
	s_mov_b64 exec, s[66:67]
	ds_write_b32 v121, v147
	s_mov_b64 exec, -1
	v_add_u32_e32 v146, 0x40000, v145
	v_and_or_b32 v146, v90, 60, v146
	s_mov_b64 exec, s[68:69]
	ds_write_b32 v122, v146
	s_mov_b64 exec, -1
	v_add_u32_e32 v147, 0x40040, v145
	v_and_or_b32 v147, v91, 60, v147
	s_mov_b64 exec, s[70:71]
	ds_write_b32 v123, v147
	s_mov_b64 exec, -1
	v_add_u32_e32 v146, 0x40080, v145
	v_and_or_b32 v146, v92, 60, v146
	s_mov_b64 exec, s[72:73]
	ds_write_b32 v124, v146
	s_mov_b64 exec, -1
	v_add_u32_e32 v147, 0x400c0, v145
	v_and_or_b32 v147, v93, 60, v147
	s_mov_b64 exec, s[74:75]
	ds_write_b32 v125, v147
	s_mov_b64 exec, -1
	v_add_u32_e32 v146, 0x50000, v145
	v_and_or_b32 v146, v94, 60, v146
	s_mov_b64 exec, s[76:77]
	ds_write_b32 v126, v146
	s_mov_b64 exec, -1
	v_add_u32_e32 v147, 0x50040, v145
	v_and_or_b32 v147, v95, 60, v147
	s_mov_b64 exec, s[78:79]
	ds_write_b32 v127, v147
	s_mov_b64 exec, -1
	v_add_u32_e32 v146, 0x50080, v145
	v_and_or_b32 v146, v96, 60, v146
	s_mov_b64 exec, s[80:81]
	ds_write_b32 v128, v146
	s_mov_b64 exec, -1
	v_add_u32_e32 v147, 0x500c0, v145
	v_and_or_b32 v147, v97, 60, v147
	s_mov_b64 exec, s[82:83]
	ds_write_b32 v129, v147
	s_mov_b64 exec, -1
	v_add_u32_e32 v146, 0x60000, v145
	v_and_or_b32 v146, v98, 60, v146
	s_mov_b64 exec, s[84:85]
	ds_write_b32 v130, v146
	s_mov_b64 exec, -1
	v_add_u32_e32 v147, 0x60040, v145
	v_and_or_b32 v147, v99, 60, v147
	s_mov_b64 exec, s[86:87]
	ds_write_b32 v131, v147
	s_mov_b64 exec, -1
	v_add_u32_e32 v146, 0x60080, v145
	v_and_or_b32 v146, v100, 60, v146
	s_mov_b64 exec, s[88:89]
	ds_write_b32 v132, v146
	s_mov_b64 exec, -1
	v_add_u32_e32 v147, 0x600c0, v145
	v_and_or_b32 v147, v101, 60, v147
	s_mov_b64 exec, s[90:91]
	ds_write_b32 v133, v147
	s_mov_b64 exec, -1
	v_add_u32_e32 v146, 0x70000, v145
	v_and_or_b32 v146, v102, 60, v146
	s_mov_b64 exec, s[92:93]
	ds_write_b32 v134, v146
	s_mov_b64 exec, -1
	v_add_u32_e32 v147, 0x70040, v145
	v_and_or_b32 v147, v103, 60, v147
	s_mov_b64 exec, s[94:95]
	ds_write_b32 v135, v147
	s_mov_b64 exec, -1
	v_add_u32_e32 v146, 0x70080, v145
	v_and_or_b32 v146, v104, 60, v146
	s_mov_b64 exec, s[96:97]
	ds_write_b32 v136, v146
	s_mov_b64 exec, -1
	v_add_u32_e32 v147, 0x700c0, v145
	v_and_or_b32 v147, v105, 60, v147
	s_mov_b64 exec, s[98:99]
	ds_write_b32 v137, v147
	s_mov_b64 exec, -1
	s_waitcnt lgkmcnt(0)
	s_barrier
	s_add_i32 s53, s8, 7
	s_lshr_b32 s53, s53, 3
	v_lshlrev_b32_e32 v218, 4, v1
	v_lshlrev_b32_e32 v219, 3, v1
	v_mov_b32_e32 v223, 0x11540
	v_and_b32_e32 v221, 15, v1
	v_mov_b32_e32 v200, 0
	v_mov_b32_e32 v201, 0
	v_mov_b32_e32 v202, 0
	v_mov_b32_e32 v203, 0
	v_mov_b32_e32 v204, 0
	v_mov_b32_e32 v205, 0
	v_mov_b32_e32 v206, 0
	v_mov_b32_e32 v207, 0
	s_mov_b32 s50, -1
	s_mov_b64 exec, 1
	ds_add_rtn_u32 v222, v223, v142
	s_mov_b64 exec, -1
	s_waitcnt lgkmcnt(0)
	v_readfirstlane_b32 s54, v222
	s_mov_b64 exec, 1
	ds_add_rtn_u32 v222, v223, v142
	s_mov_b64 exec, -1
	s_waitcnt lgkmcnt(0)
	v_readfirstlane_b32 s55, v222
	s_cmp_ge_u32 s54, s53
	s_cbranch_scc1 .Lg_nochunk
	s_lshl_b32 s46, s54, 3
	v_add_u32_e32 v220, s46, v221
	v_cmp_gt_u32_e32 vcc, s8, v220
	v_lshlrev_b32_e32 v220, 2, v220
	ds_read_b32 v216, v220
	s_waitcnt lgkmcnt(0)
	v_cndmask_b32_e32 v216, 1, v216, vcc
	s_nop 1
	v_readlane_b32 s50, v216, 0
	s_bfe_u32 s50, s50, 0x40002
	v_readlane_b32 s40, v216, 0
	s_bfe_u32 s60, s40, 0x40002
	s_bitcmp1_b32 s40, 0
	s_cselect_b32 s60, 16, s60
	s_and_b32 s40, s40, 0xffffffc0
	s_lshl_b32 s40, s40, 4
	s_add_u32 s42, s32, s40
	s_addc_u32 s43, s33, 0
	global_load_dwordx4 v[66:69], v218, s[42:43] nt
	v_readlane_b32 s40, v216, 1
	s_bfe_u32 s61, s40, 0x40002
	s_bitcmp1_b32 s40, 0
	s_cselect_b32 s61, 16, s61
	s_and_b32 s40, s40, 0xffffffc0
	s_lshl_b32 s40, s40, 4
	s_add_u32 s42, s32, s40
	s_addc_u32 s43, s33, 0
	global_load_dwordx4 v[70:73], v218, s[42:43] nt
	v_readlane_b32 s40, v216, 2
	s_bfe_u32 s62, s40, 0x40002
	s_bitcmp1_b32 s40, 0
	s_cselect_b32 s62, 16, s62
	s_and_b32 s40, s40, 0xffffffc0
	s_lshl_b32 s40, s40, 4
	s_add_u32 s42, s32, s40
	s_addc_u32 s43, s33, 0
	global_load_dwordx4 v[74:77], v218, s[42:43] nt
	v_readlane_b32 s40, v216, 3
	s_bfe_u32 s63, s40, 0x40002
	s_bitcmp1_b32 s40, 0
	s_cselect_b32 s63, 16, s63
	s_and_b32 s40, s40, 0xffffffc0
	s_lshl_b32 s40, s40, 4
	s_add_u32 s42, s32, s40
	s_addc_u32 s43, s33, 0
	global_load_dwordx4 v[78:81], v218, s[42:43] nt
	v_readlane_b32 s40, v216, 4
	s_bfe_u32 s64, s40, 0x40002
	s_bitcmp1_b32 s40, 0
	s_cselect_b32 s64, 16, s64
	s_and_b32 s40, s40, 0xffffffc0
	s_lshl_b32 s40, s40, 4
	s_add_u32 s42, s32, s40
	s_addc_u32 s43, s33, 0
	global_load_dwordx4 v[82:85], v218, s[42:43] nt
	v_readlane_b32 s40, v216, 5
	s_bfe_u32 s65, s40, 0x40002
	s_bitcmp1_b32 s40, 0
	s_cselect_b32 s65, 16, s65
	s_and_b32 s40, s40, 0xffffffc0
	s_lshl_b32 s40, s40, 4
	s_add_u32 s42, s32, s40
	s_addc_u32 s43, s33, 0
	global_load_dwordx4 v[86:89], v218, s[42:43] nt
	v_readlane_b32 s40, v216, 6
	s_bfe_u32 s66, s40, 0x40002
	s_bitcmp1_b32 s40, 0
	s_cselect_b32 s66, 16, s66
	s_and_b32 s40, s40, 0xffffffc0
	s_lshl_b32 s40, s40, 4
	s_add_u32 s42, s32, s40
	s_addc_u32 s43, s33, 0
	global_load_dwordx4 v[90:93], v218, s[42:43] nt
	v_readlane_b32 s40, v216, 7
	s_bfe_u32 s67, s40, 0x40002
	s_bitcmp1_b32 s40, 0
	s_cselect_b32 s67, 16, s67
	s_and_b32 s40, s40, 0xffffffc0
	s_lshl_b32 s40, s40, 4
	s_add_u32 s42, s32, s40
	s_addc_u32 s43, s33, 0
	global_load_dwordx4 v[94:97], v218, s[42:43] nt
	s_cmp_ge_u32 s55, s53
	s_cbranch_scc1 .Lg_noB
	s_lshl_b32 s46, s55, 3
	v_add_u32_e32 v220, s46, v221
	v_cmp_gt_u32_e32 vcc, s8, v220
	v_lshlrev_b32_e32 v220, 2, v220
	ds_read_b32 v217, v220
	s_waitcnt lgkmcnt(0)
	v_cndmask_b32_e32 v217, 1, v217, vcc
	s_nop 1
	v_readlane_b32 s40, v217, 0
	s_bfe_u32 s68, s40, 0x40002
	s_bitcmp1_b32 s40, 0
	s_cselect_b32 s68, 16, s68
	s_and_b32 s40, s40, 0xffffffc0
	s_lshl_b32 s40, s40, 4
	s_add_u32 s42, s32, s40
	s_addc_u32 s43, s33, 0
	global_load_dwordx4 v[98:101], v218, s[42:43] nt
	v_readlane_b32 s40, v217, 1
	s_bfe_u32 s69, s40, 0x40002
	s_bitcmp1_b32 s40, 0
	s_cselect_b32 s69, 16, s69
	s_and_b32 s40, s40, 0xffffffc0
	s_lshl_b32 s40, s40, 4
	s_add_u32 s42, s32, s40
	s_addc_u32 s43, s33, 0
	global_load_dwordx4 v[102:105], v218, s[42:43] nt
	v_readlane_b32 s40, v217, 2
	s_bfe_u32 s70, s40, 0x40002
	s_bitcmp1_b32 s40, 0
	s_cselect_b32 s70, 16, s70
	s_and_b32 s40, s40, 0xffffffc0
	s_lshl_b32 s40, s40, 4
	s_add_u32 s42, s32, s40
	s_addc_u32 s43, s33, 0
	global_load_dwordx4 v[106:109], v218, s[42:43] nt
	v_readlane_b32 s40, v217, 3
	s_bfe_u32 s71, s40, 0x40002
	s_bitcmp1_b32 s40, 0
	s_cselect_b32 s71, 16, s71
	s_and_b32 s40, s40, 0xffffffc0
	s_lshl_b32 s40, s40, 4
	s_add_u32 s42, s32, s40
	s_addc_u32 s43, s33, 0
	global_load_dwordx4 v[110:113], v218, s[42:43] nt
	v_readlane_b32 s40, v217, 4
	s_bfe_u32 s72, s40, 0x40002
	s_bitcmp1_b32 s40, 0
	s_cselect_b32 s72, 16, s72
	s_and_b32 s40, s40, 0xffffffc0
	s_lshl_b32 s40, s40, 4
	s_add_u32 s42, s32, s40
	s_addc_u32 s43, s33, 0
	global_load_dwordx4 v[114:117], v218, s[42:43] nt
	v_readlane_b32 s40, v217, 5
	s_bfe_u32 s73, s40, 0x40002
	s_bitcmp1_b32 s40, 0
	s_cselect_b32 s73, 16, s73
	s_and_b32 s40, s40, 0xffffffc0
	s_lshl_b32 s40, s40, 4
	s_add_u32 s42, s32, s40
	s_addc_u32 s43, s33, 0
	global_load_dwordx4 v[118:121], v218, s[42:43] nt
	v_readlane_b32 s40, v217, 6
	s_bfe_u32 s74, s40, 0x40002
	s_bitcmp1_b32 s40, 0
	s_cselect_b32 s74, 16, s74
	s_and_b32 s40, s40, 0xffffffc0
	s_lshl_b32 s40, s40, 4
	s_add_u32 s42, s32, s40
	s_addc_u32 s43, s33, 0
	global_load_dwordx4 v[122:125], v218, s[42:43] nt
	v_readlane_b32 s40, v217, 7
	s_bfe_u32 s75, s40, 0x40002
	s_bitcmp1_b32 s40, 0
	s_cselect_b32 s75, 16, s75
	s_and_b32 s40, s40, 0xffffffc0
	s_lshl_b32 s40, s40, 4
	s_add_u32 s42, s32, s40
	s_addc_u32 s43, s33, 0
	global_load_dwordx4 v[126:129], v218, s[42:43] nt
	s_waitcnt vmcnt(16)
	v_mul_f32_e32 v150, v62, v62
	v_mul_f32_e32 v151, v63, v63
	v_mul_f32_e32 v152, v64, v64
	v_mul_f32_e32 v153, v65, v65
	v_fmac_f32_e32 v150, v58, v58
	v_fmac_f32_e32 v151, v59, v59
	v_fmac_f32_e32 v152, v60, v60
	v_fmac_f32_e32 v153, v61, v61
	v_fmac_f32_e32 v150, v54, v54
	v_fmac_f32_e32 v151, v55, v55
	v_fmac_f32_e32 v152, v56, v56
	v_fmac_f32_e32 v153, v57, v57
	v_fmac_f32_e32 v150, v50, v50
	v_fmac_f32_e32 v151, v51, v51
	v_fmac_f32_e32 v152, v52, v52
	v_fmac_f32_e32 v153, v53, v53
	v_fmac_f32_e32 v150, v46, v46
	v_fmac_f32_e32 v151, v47, v47
	v_fmac_f32_e32 v152, v48, v48
	v_fmac_f32_e32 v153, v49, v49
	v_fmac_f32_e32 v150, v42, v42
	v_fmac_f32_e32 v151, v43, v43
	v_fmac_f32_e32 v152, v44, v44
	v_fmac_f32_e32 v153, v45, v45
	v_fmac_f32_e32 v150, v38, v38
	v_fmac_f32_e32 v151, v39, v39
	v_fmac_f32_e32 v152, v40, v40
	v_fmac_f32_e32 v153, v41, v41
	v_fmac_f32_e32 v150, v34, v34
	v_fmac_f32_e32 v151, v35, v35
	v_fmac_f32_e32 v152, v36, v36
	v_fmac_f32_e32 v153, v37, v37
	v_fmac_f32_e32 v150, v30, v30
	v_fmac_f32_e32 v151, v31, v31
	v_fmac_f32_e32 v152, v32, v32
	v_fmac_f32_e32 v153, v33, v33
	v_fmac_f32_e32 v150, v26, v26
	v_fmac_f32_e32 v151, v27, v27
	v_fmac_f32_e32 v152, v28, v28
	v_fmac_f32_e32 v153, v29, v29
	v_fmac_f32_e32 v150, v22, v22
	v_fmac_f32_e32 v151, v23, v23
	v_fmac_f32_e32 v152, v24, v24
	v_fmac_f32_e32 v153, v25, v25
	v_fmac_f32_e32 v150, v18, v18
	v_fmac_f32_e32 v151, v19, v19
	v_fmac_f32_e32 v152, v20, v20
	v_fmac_f32_e32 v153, v21, v21
	v_fmac_f32_e32 v150, v14, v14
	v_fmac_f32_e32 v151, v15, v15
	v_fmac_f32_e32 v152, v16, v16
	v_fmac_f32_e32 v153, v17, v17
	v_fmac_f32_e32 v150, v10, v10
	v_fmac_f32_e32 v151, v11, v11
	v_fmac_f32_e32 v152, v12, v12
	v_fmac_f32_e32 v153, v13, v13
	v_fmac_f32_e32 v150, v6, v6
	v_fmac_f32_e32 v151, v7, v7
	v_fmac_f32_e32 v152, v8, v8
	v_fmac_f32_e32 v153, v9, v9
	v_fmac_f32_e32 v150, v2, v2
	v_fmac_f32_e32 v151, v3, v3
	v_fmac_f32_e32 v152, v4, v4
	v_fmac_f32_e32 v153, v5, v5
	v_add_f32_e32 v150, v150, v151
	v_add_f32_e32 v152, v152, v153
	v_add_f32_e32 v150, v150, v152
	v_mbcnt_lo_u32_b32 v151, -1, 0
	v_mbcnt_hi_u32_b32 v151, -1, v151
	v_xor_b32_e32 v152, 16, v151
	v_lshlrev_b32_e32 v152, 2, v152
	ds_bpermute_b32 v152, v152, v150
	v_xor_b32_e32 v153, 32, v151
	v_lshlrev_b32_e32 v153, 2, v153
	s_waitcnt lgkmcnt(0)
	v_add_f32_e32 v150, v150, v152
	ds_bpermute_b32 v153, v153, v150
	v_add_u32_e32 v152, s24, v1
	v_lshlrev_b32_e32 v152, 2, v152
	v_add_u32_e32 v152, 0x11300, v152
	v_cmp_gt_u32_e32 vcc, 16, v1
	s_and_saveexec_b64 s[30:31], vcc
	s_waitcnt lgkmcnt(0)
	v_add_f32_e32 v150, v150, v153
	ds_write_b32 v152, v150
	s_mov_b64 exec, s[30:31]

.LBB0_118:
	s_waitcnt vmcnt(0)
	v_lshrrev_b32_e32 v67, 4, v0
	v_mov_b32_e32 v66, 0x11100
	v_lshl_or_b32 v66, v67, 2, v66
	s_waitcnt lgkmcnt(0)
	s_barrier
	ds_read_b32 v66, v66
	v_mul_u32_u24_e32 v68, 0x102, v67
	v_lshlrev_b32_e32 v72, 3, v68
	s_waitcnt lgkmcnt(0)
	v_max_i32_e32 v66, 1, v66
	v_cvt_f32_u32_e32 v66, v66
	v_div_scale_f32 v69, s[0:1], v66, v66, 1.0
	v_rcp_f32_e32 v70, v69
	v_div_scale_f32 v68, vcc, 1.0, v66, 1.0
	v_fma_f32 v71, -v69, v70, 1.0
	v_fmac_f32_e32 v70, v71, v70
	v_mul_f32_e32 v71, v68, v70
	v_fma_f32 v73, -v69, v71, v68
	v_fmac_f32_e32 v71, v73, v70
	v_fma_f32 v68, -v69, v71, v68
	v_div_fmas_f32 v73, v68, v70, v71
	v_lshl_add_u32 v68, v138, 3, v72
	v_add_u32_e32 v76, 0x8000, v68
	ds_read2_b64 v[68:71], v76 offset1:16
	v_div_fixup_f32 v77, v73, v66, 1.0
	v_mul_i32_i24_e32 v73, 0xfffffbf8, v67
	v_lshlrev_b32_e32 v66, 2, v138
	v_add3_u32 v78, v72, v73, v66
	ds_read2_b64 v[72:75], v76 offset0:32 offset1:48
	s_waitcnt lgkmcnt(1)
	v_cvt_f32_f64_e32 v68, v[68:69]
	v_cvt_f32_f64_e32 v69, v[70:71]
	v_mul_f32_e32 v68, v77, v68
	v_mul_f32_e32 v69, v77, v69
	v_fma_f32 v79, v68, v68, 0
	ds_write2_b32 v78, v68, v69 offset1:16
	s_waitcnt lgkmcnt(1)
	v_cvt_f32_f64_e32 v68, v[72:73]
	v_fmac_f32_e32 v79, v69, v69
	v_mul_f32_e32 v72, v77, v68
	ds_read2_b64 v[68:71], v76 offset0:64 offset1:80
	v_cvt_f32_f64_e32 v73, v[74:75]
	v_fmac_f32_e32 v79, v72, v72
	v_mul_f32_e32 v73, v77, v73
	v_fmac_f32_e32 v79, v73, v73
	ds_write2_b32 v78, v72, v73 offset0:32 offset1:48
	ds_read2_b64 v[72:75], v76 offset0:96 offset1:112
	s_waitcnt lgkmcnt(2)
	v_cvt_f32_f64_e32 v68, v[68:69]
	v_cvt_f32_f64_e32 v69, v[70:71]
	v_mul_f32_e32 v68, v77, v68
	v_mul_f32_e32 v69, v77, v69
	v_fmac_f32_e32 v79, v68, v68
	ds_write2_b32 v78, v68, v69 offset0:64 offset1:80
	s_waitcnt lgkmcnt(1)
	v_cvt_f32_f64_e32 v68, v[72:73]
	v_fmac_f32_e32 v79, v69, v69
	v_mul_f32_e32 v72, v77, v68
	ds_read2_b64 v[68:71], v76 offset0:128 offset1:144
	v_cvt_f32_f64_e32 v73, v[74:75]
	v_fmac_f32_e32 v79, v72, v72
	v_mul_f32_e32 v73, v77, v73
	v_fmac_f32_e32 v79, v73, v73
	ds_write2_b32 v78, v72, v73 offset0:96 offset1:112
	ds_read2_b64 v[72:75], v76 offset0:160 offset1:176
	s_waitcnt lgkmcnt(2)
	v_cvt_f32_f64_e32 v68, v[68:69]
	v_cvt_f32_f64_e32 v69, v[70:71]
	v_mul_f32_e32 v68, v77, v68
	v_mul_f32_e32 v69, v77, v69
	v_fmac_f32_e32 v79, v68, v68
	ds_write2_b32 v78, v68, v69 offset0:128 offset1:144
	s_waitcnt lgkmcnt(1)
	v_cvt_f32_f64_e32 v68, v[72:73]
	v_fmac_f32_e32 v79, v69, v69
	v_mul_f32_e32 v72, v77, v68
	ds_read2_b64 v[68:71], v76 offset0:192 offset1:208
	v_cvt_f32_f64_e32 v73, v[74:75]
	v_fmac_f32_e32 v79, v72, v72
	v_mul_f32_e32 v73, v77, v73
	v_fmac_f32_e32 v79, v73, v73
	ds_write2_b32 v78, v72, v73 offset0:160 offset1:176
	ds_read2_b64 v[72:75], v76 offset0:224 offset1:240
	s_waitcnt lgkmcnt(2)
	v_cvt_f32_f64_e32 v68, v[68:69]
	v_cvt_f32_f64_e32 v69, v[70:71]
	v_mul_f32_e32 v68, v77, v68
	v_mul_f32_e32 v69, v77, v69
	v_fmac_f32_e32 v79, v68, v68
	ds_write2_b32 v78, v68, v69 offset0:192 offset1:208
	s_waitcnt lgkmcnt(1)
	v_cvt_f32_f64_e32 v68, v[72:73]
	v_fmac_f32_e32 v79, v69, v69
	v_mul_f32_e32 v68, v77, v68
	v_cvt_f32_f64_e32 v69, v[74:75]
	v_fmac_f32_e32 v79, v68, v68
	v_mul_f32_e32 v69, v77, v69
	v_fmac_f32_e32 v79, v69, v69
	ds_write2_b32 v78, v68, v69 offset0:224 offset1:240
	v_cmp_eq_u32_e32 vcc, 0, v138
	v_add_f32_dpp v68, v79, v79 quad_perm:[1,0,3,2] row_mask:0xf bank_mask:0xf bound_ctrl:1
	s_nop 1
	v_add_f32_dpp v68, v68, v68 quad_perm:[2,3,0,1] row_mask:0xf bank_mask:0xf bound_ctrl:1
	s_nop 1
	v_add_f32_dpp v68, v68, v68 row_half_mirror row_mask:0xf bank_mask:0xf bound_ctrl:1
	s_nop 1
	v_mov_b32_dpp v69, v68 row_mirror row_mask:0xf bank_mask:0xf bound_ctrl:1
	s_and_saveexec_b64 s[0:1], vcc
	v_mov_b32_e32 v70, 0x11200
	v_lshl_or_b32 v67, v67, 2, v70
	v_add_f32_e32 v68, v68, v69
	ds_write_b32 v67, v68
	s_or_b64 exec, exec, s[0:1]
	v_lshlrev_b32_e32 v67, 2, v140
	s_movk_i32 s0, 0x408
	v_mad_u32_u24 v67, v138, s0, v67
	s_waitcnt lgkmcnt(0)
	s_barrier
	ds_read2_b32 v[68:69], v67 offset1:4
	ds_read2_b32 v[70:71], v67 offset0:64 offset1:68
	ds_read2_b32 v[72:73], v67 offset0:192 offset1:196
	s_lshl_b32 s29, s17, 2
	s_lshl_b32 s0, s24, 2
	s_waitcnt lgkmcnt(2)
	v_mfma_f32_16x16x4_f32 a[0:3], v68, v62, 0
	s_add_i32 s0, s0, 0x10100
	s_waitcnt lgkmcnt(1)
	v_mfma_f32_16x16x4_f32 a[0:3], v70, v63, a[0:3]
	ds_read2_b32 v[62:63], v67 offset0:128 offset1:132
	s_waitcnt lgkmcnt(0)
	v_mfma_f32_16x16x4_f32 a[0:3], v62, v64, a[0:3]
	v_mfma_f32_16x16x4_f32 a[0:3], v72, v65, a[0:3]
	v_mfma_f32_16x16x4_f32 a[0:3], v69, v58, a[0:3]
	v_mfma_f32_16x16x4_f32 a[0:3], v71, v59, a[0:3]
	ds_read2_b32 v[58:59], v67 offset0:8 offset1:12
	v_mfma_f32_16x16x4_f32 a[0:3], v63, v60, a[0:3]
	ds_read2_b32 v[62:63], v67 offset0:200 offset1:204
	v_mfma_f32_16x16x4_f32 a[0:3], v73, v61, a[0:3]
	ds_read2_b32 v[60:61], v67 offset0:72 offset1:76
	s_waitcnt lgkmcnt(2)
	v_mfma_f32_16x16x4_f32 a[0:3], v58, v54, a[0:3]
	s_waitcnt lgkmcnt(0)
	v_mfma_f32_16x16x4_f32 a[0:3], v60, v55, a[0:3]
	ds_read2_b32 v[54:55], v67 offset0:136 offset1:140
	s_waitcnt lgkmcnt(0)
	v_mfma_f32_16x16x4_f32 a[0:3], v54, v56, a[0:3]
	v_mfma_f32_16x16x4_f32 a[0:3], v62, v57, a[0:3]
	v_mfma_f32_16x16x4_f32 a[0:3], v59, v50, a[0:3]
	v_mfma_f32_16x16x4_f32 a[0:3], v61, v51, a[0:3]
	ds_read2_b32 v[50:51], v67 offset0:16 offset1:20
	v_mfma_f32_16x16x4_f32 a[0:3], v55, v52, a[0:3]
	ds_read2_b32 v[54:55], v67 offset0:208 offset1:212
	v_mfma_f32_16x16x4_f32 a[0:3], v63, v53, a[0:3]
	ds_read2_b32 v[52:53], v67 offset0:80 offset1:84
	s_waitcnt lgkmcnt(2)
	v_mfma_f32_16x16x4_f32 a[0:3], v50, v46, a[0:3]
	s_waitcnt lgkmcnt(0)
	v_mfma_f32_16x16x4_f32 a[0:3], v52, v47, a[0:3]
	ds_read2_b32 v[46:47], v67 offset0:144 offset1:148
	s_waitcnt lgkmcnt(0)
	v_mfma_f32_16x16x4_f32 a[0:3], v46, v48, a[0:3]
	v_mfma_f32_16x16x4_f32 a[0:3], v54, v49, a[0:3]
	v_mfma_f32_16x16x4_f32 a[0:3], v51, v42, a[0:3]
	v_mfma_f32_16x16x4_f32 a[0:3], v53, v43, a[0:3]
	ds_read2_b32 v[42:43], v67 offset0:24 offset1:28
	v_mfma_f32_16x16x4_f32 a[0:3], v47, v44, a[0:3]
	ds_read2_b32 v[46:47], v67 offset0:216 offset1:220
	v_mfma_f32_16x16x4_f32 a[0:3], v55, v45, a[0:3]
	ds_read2_b32 v[44:45], v67 offset0:88 offset1:92
	s_waitcnt lgkmcnt(2)
	v_mfma_f32_16x16x4_f32 a[0:3], v42, v38, a[0:3]
	s_waitcnt lgkmcnt(0)
	v_mfma_f32_16x16x4_f32 a[0:3], v44, v39, a[0:3]
	ds_read2_b32 v[38:39], v67 offset0:152 offset1:156
	s_waitcnt lgkmcnt(0)
	v_mfma_f32_16x16x4_f32 a[0:3], v38, v40, a[0:3]
	v_mfma_f32_16x16x4_f32 a[0:3], v46, v41, a[0:3]
	v_mfma_f32_16x16x4_f32 a[0:3], v43, v34, a[0:3]
	v_mfma_f32_16x16x4_f32 a[0:3], v45, v35, a[0:3]
	ds_read2_b32 v[34:35], v67 offset0:32 offset1:36
	v_mfma_f32_16x16x4_f32 a[0:3], v39, v36, a[0:3]
	ds_read2_b32 v[38:39], v67 offset0:224 offset1:228
	v_mfma_f32_16x16x4_f32 a[0:3], v47, v37, a[0:3]
	ds_read2_b32 v[36:37], v67 offset0:96 offset1:100
	s_waitcnt lgkmcnt(2)
	v_mfma_f32_16x16x4_f32 a[0:3], v34, v30, a[0:3]
	s_waitcnt lgkmcnt(0)
	v_mfma_f32_16x16x4_f32 a[0:3], v36, v31, a[0:3]
	ds_read2_b32 v[30:31], v67 offset0:160 offset1:164
	s_waitcnt lgkmcnt(0)
	v_mfma_f32_16x16x4_f32 a[0:3], v30, v32, a[0:3]
	v_mfma_f32_16x16x4_f32 a[0:3], v38, v33, a[0:3]
	v_mfma_f32_16x16x4_f32 a[0:3], v35, v26, a[0:3]
	v_mfma_f32_16x16x4_f32 a[0:3], v37, v27, a[0:3]
	ds_read2_b32 v[26:27], v67 offset0:40 offset1:44
	v_mfma_f32_16x16x4_f32 a[0:3], v31, v28, a[0:3]
	ds_read2_b32 v[30:31], v67 offset0:232 offset1:236
	v_mfma_f32_16x16x4_f32 a[0:3], v39, v29, a[0:3]
	ds_read2_b32 v[28:29], v67 offset0:104 offset1:108
	s_waitcnt lgkmcnt(2)
	v_mfma_f32_16x16x4_f32 a[0:3], v26, v22, a[0:3]
	s_waitcnt lgkmcnt(0)
	v_mfma_f32_16x16x4_f32 a[0:3], v28, v23, a[0:3]
	ds_read2_b32 v[22:23], v67 offset0:168 offset1:172
	s_waitcnt lgkmcnt(0)
	v_mfma_f32_16x16x4_f32 a[0:3], v22, v24, a[0:3]
	v_mfma_f32_16x16x4_f32 a[0:3], v30, v25, a[0:3]
	v_mfma_f32_16x16x4_f32 a[0:3], v27, v18, a[0:3]
	v_mfma_f32_16x16x4_f32 a[0:3], v29, v19, a[0:3]
	ds_read2_b32 v[18:19], v67 offset0:48 offset1:52
	v_mfma_f32_16x16x4_f32 a[0:3], v23, v20, a[0:3]
	ds_read2_b32 v[22:23], v67 offset0:240 offset1:244
	v_mfma_f32_16x16x4_f32 a[0:3], v31, v21, a[0:3]
	ds_read2_b32 v[20:21], v67 offset0:112 offset1:116
	s_waitcnt lgkmcnt(2)
	v_mfma_f32_16x16x4_f32 a[0:3], v18, v14, a[0:3]
	s_waitcnt lgkmcnt(0)
	v_mfma_f32_16x16x4_f32 a[0:3], v20, v15, a[0:3]
	ds_read2_b32 v[14:15], v67 offset0:176 offset1:180
	s_waitcnt lgkmcnt(0)
	v_mfma_f32_16x16x4_f32 a[0:3], v14, v16, a[0:3]
	v_mfma_f32_16x16x4_f32 a[0:3], v22, v17, a[0:3]
	v_mfma_f32_16x16x4_f32 a[0:3], v19, v10, a[0:3]
	v_mfma_f32_16x16x4_f32 a[0:3], v21, v11, a[0:3]
	ds_read2_b32 v[10:11], v67 offset0:56 offset1:60
	v_mfma_f32_16x16x4_f32 a[0:3], v15, v12, a[0:3]
	ds_read2_b32 v[14:15], v67 offset0:248 offset1:252
	v_mfma_f32_16x16x4_f32 a[0:3], v23, v13, a[0:3]
	ds_read2_b32 v[12:13], v67 offset0:120 offset1:124
	s_waitcnt lgkmcnt(2)
	v_mfma_f32_16x16x4_f32 a[0:3], v10, v6, a[0:3]
	s_waitcnt lgkmcnt(0)
	v_mfma_f32_16x16x4_f32 a[0:3], v12, v7, a[0:3]
	ds_read2_b32 v[6:7], v67 offset0:184 offset1:188
	s_waitcnt lgkmcnt(0)
	v_mfma_f32_16x16x4_f32 a[0:3], v6, v8, a[0:3]
	v_mfma_f32_16x16x4_f32 a[0:3], v14, v9, a[0:3]
	v_mfma_f32_16x16x4_f32 a[0:3], v11, v2, a[0:3]
	v_mov_b32_e32 v2, 0x11300
	v_lshl_add_u32 v2, v134, 2, v2
	ds_read_b32 v2, v2
	v_mfma_f32_16x16x4_f32 a[0:3], v13, v3, a[0:3]
	v_lshlrev_b32_e32 v3, 10, v140
	v_add3_u32 v3, s0, v66, v3
	v_mfma_f32_16x16x4_f32 a[0:3], v7, v4, a[0:3]
	v_or_b32_e32 v7, s29, v140
	v_lshl_or_b32 v4, v7, 8, v66
	v_add_u32_e32 v4, 0x10100, v4
	v_mfma_f32_16x16x4_f32 a[0:3], v15, v5, a[0:3]
	s_nop 9
	v_accvgpr_read_b32 v5, a0
	v_accvgpr_read_b32 v6, a1
	v_accvgpr_read_b32 v8, a2
	v_accvgpr_read_b32 v9, a3
	s_waitcnt lgkmcnt(0)
	v_fma_f32 v5, -2.0, v5, v2
	v_fma_f32 v6, -2.0, v6, v2
	v_fma_f32 v8, -2.0, v8, v2
	v_fmac_f32_e32 v2, -2.0, v9
	ds_write2st64_b32 v3, v5, v6 offset1:1
	ds_write2st64_b32 v3, v8, v2 offset0:2 offset1:3
	s_waitcnt lgkmcnt(0)
	s_barrier
	ds_read2_b32 v[2:3], v4 offset1:16
	ds_read2_b32 v[4:5], v4 offset0:32 offset1:48
	v_or_b32_e32 v6, 16, v138
	v_or_b32_e32 v8, 32, v138
	v_or_b32_e32 v9, 48, v138
	s_waitcnt lgkmcnt(1)
	v_cmp_lt_f32_e32 vcc, v3, v2
	s_nop 1
	v_cndmask_b32_e32 v10, v2, v3, vcc
	v_cndmask_b32_e32 v6, v138, v6, vcc
	s_waitcnt lgkmcnt(0)
	v_cmp_lt_f32_e32 vcc, v4, v10
	s_nop 1
	v_cndmask_b32_e32 v10, v10, v4, vcc
	v_cndmask_b32_e32 v8, v6, v8, vcc
	v_cmp_lt_f32_e32 vcc, v5, v10
	s_nop 1
	v_cndmask_b32_e32 v6, v10, v5, vcc
	v_cndmask_b32_e32 v14, v8, v9, vcc
	s_nop 0
	v_mov_b32_dpp v9, v6 quad_perm:[1,0,3,2] row_mask:0xf bank_mask:0xf bound_ctrl:1
	v_mov_b32_dpp v8, v14 quad_perm:[1,0,3,2] row_mask:0xf bank_mask:0xf bound_ctrl:1
	v_cmp_gt_f32_e64 s[4:5], v6, v9
	v_cmp_ngt_f32_e32 vcc, v6, v9
	s_and_saveexec_b64 s[6:7], vcc
	v_cmp_eq_f32_e32 vcc, v6, v9
	v_cmp_lt_i32_e64 s[0:1], v8, v14
	s_and_b64 s[0:1], vcc, s[0:1]
	s_andn2_b64 s[4:5], s[4:5], exec
	s_and_b64 s[0:1], s[0:1], exec
	s_or_b64 s[4:5], s[4:5], s[0:1]
	s_or_b64 exec, exec, s[6:7]
	s_and_saveexec_b64 s[0:1], s[4:5]
	v_mov_b32_e32 v6, v9
	v_mov_b32_e32 v14, v8
	s_or_b64 exec, exec, s[0:1]
	v_mov_b32_dpp v9, v6 quad_perm:[2,3,0,1] row_mask:0xf bank_mask:0xf bound_ctrl:1
	v_mov_b32_dpp v8, v14 quad_perm:[2,3,0,1] row_mask:0xf bank_mask:0xf bound_ctrl:1
	v_cmp_gt_f32_e64 s[4:5], v6, v9
	v_cmp_ngt_f32_e32 vcc, v6, v9
	s_and_saveexec_b64 s[6:7], vcc
	v_cmp_eq_f32_e32 vcc, v6, v9
	v_cmp_lt_i32_e64 s[0:1], v8, v14
	s_and_b64 s[0:1], vcc, s[0:1]
	s_andn2_b64 s[4:5], s[4:5], exec
	s_and_b64 s[0:1], s[0:1], exec
	s_or_b64 s[4:5], s[4:5], s[0:1]
	s_or_b64 exec, exec, s[6:7]
	s_and_saveexec_b64 s[0:1], s[4:5]
	v_mov_b32_e32 v6, v9
	v_mov_b32_e32 v14, v8
	s_or_b64 exec, exec, s[0:1]
	v_mov_b32_dpp v9, v6 row_half_mirror row_mask:0xf bank_mask:0xf bound_ctrl:1
	v_mov_b32_dpp v8, v14 row_half_mirror row_mask:0xf bank_mask:0xf bound_ctrl:1
	v_cmp_gt_f32_e64 s[4:5], v6, v9
	v_cmp_ngt_f32_e32 vcc, v6, v9
	s_and_saveexec_b64 s[6:7], vcc
	v_cmp_eq_f32_e32 vcc, v6, v9
	v_cmp_lt_i32_e64 s[0:1], v8, v14
	s_and_b64 s[0:1], vcc, s[0:1]
	s_andn2_b64 s[4:5], s[4:5], exec
	s_and_b64 s[0:1], s[0:1], exec
	s_or_b64 s[4:5], s[4:5], s[0:1]
	s_or_b64 exec, exec, s[6:7]
	s_and_saveexec_b64 s[0:1], s[4:5]
	v_mov_b32_e32 v6, v9
	v_mov_b32_e32 v14, v8
	s_or_b64 exec, exec, s[0:1]
	v_mov_b32_dpp v8, v6 row_mirror row_mask:0xf bank_mask:0xf bound_ctrl:1
	v_mov_b32_dpp v9, v14 row_mirror row_mask:0xf bank_mask:0xf bound_ctrl:1
	v_cmp_gt_f32_e64 s[4:5], v6, v8
	v_cmp_ngt_f32_e32 vcc, v6, v8
	s_and_saveexec_b64 s[6:7], vcc
	v_cmp_eq_f32_e32 vcc, v6, v8
	v_cmp_lt_i32_e64 s[0:1], v9, v14
	s_and_b64 s[0:1], vcc, s[0:1]
	s_andn2_b64 s[4:5], s[4:5], exec
	s_and_b64 s[0:1], s[0:1], exec
	s_or_b64 s[4:5], s[4:5], s[0:1]
	s_or_b64 exec, exec, s[6:7]
	s_and_saveexec_b64 s[0:1], s[4:5]
	v_mov_b32_e32 v6, v8
	v_mov_b32_e32 v14, v9
	s_or_b64 exec, exec, s[0:1]
	v_lshlrev_b32_e32 v86, 2, v139
	v_readlane_b32 s92, v14, 0
	s_lshl_b32 s92, s92, 10
	s_add_u32 s92, s22, s92
	s_addc_u32 s93, s23, 0
	global_load_dwordx4 v[88:91], v86, s[92:93]
	v_readlane_b32 s92, v14, 16
	s_lshl_b32 s92, s92, 10
	s_add_u32 s92, s22, s92
	s_addc_u32 s93, s23, 0
	global_load_dwordx4 v[88:91], v86, s[92:93]
	v_readlane_b32 s92, v14, 32
	s_lshl_b32 s92, s92, 10
	s_add_u32 s92, s22, s92
	s_addc_u32 s93, s23, 0
	global_load_dwordx4 v[88:91], v86, s[92:93]
	v_readlane_b32 s92, v14, 48
	s_lshl_b32 s92, s92, 10
	s_add_u32 s92, s22, s92
	s_addc_u32 s93, s23, 0
	global_load_dwordx4 v[88:91], v86, s[92:93]
	v_mov_b32_e32 v8, 0x11300
	v_lshl_or_b32 v8, v1, 2, v8
	ds_read_b32 v8, v8
	v_mov_b32_e32 v9, 0x11200
	v_lshl_add_u32 v7, v7, 2, v9
	ds_read_b32 v9, v7
	v_mov_b32_e32 v13, 0x260
	s_waitcnt lgkmcnt(1)
	v_mov_b32_dpp v7, v8 quad_perm:[1,0,3,2] row_mask:0xf bank_mask:0xf bound_ctrl:1
	v_max_f32_e32 v8, v8, v8
	v_max_f32_e32 v7, v7, v7
	v_max_f32_e32 v7, v8, v7
	v_lshlrev_b32_e32 v18, 2, v139
	v_mov_b32_e32 v19, 0
	v_mov_b32_dpp v8, v7 quad_perm:[2,3,0,1] row_mask:0xf bank_mask:0xf bound_ctrl:1
	v_max_f32_e32 v8, v8, v8
	v_max_f32_e32 v7, v7, v8
	s_mov_b32 s25, 0
	s_mov_b32 s26, s25
	v_mov_b32_dpp v8, v7 row_half_mirror row_mask:0xf bank_mask:0xf bound_ctrl:1
	v_max_f32_e32 v8, v8, v8
	v_max_f32_e32 v7, v7, v8
	s_nop 1
	v_mov_b32_dpp v8, v7 row_mirror row_mask:0xf bank_mask:0xf bound_ctrl:1
	v_max_f32_e32 v8, v8, v8
	v_max_f32_e32 v7, v7, v8
	s_nop 0
	v_readlane_b32 s4, v7, 32
	v_readlane_b32 s5, v7, 48
	v_readlane_b32 s0, v7, 0
	v_readlane_b32 s1, v7, 16
	v_max_f32_e64 v7, s5, s5
	v_max_f32_e64 v8, s4, s4
	v_max_f32_e32 v7, v8, v7
	v_mov_b32_e32 v8, s1
	v_max3_f32 v8, s0, v8, v7
	s_mov_b32 s0, 0x3f800347
	s_mov_b32 s1, 0x3f8020c5
	s_waitcnt lgkmcnt(0)
	v_pk_mul_f32 v[8:9], v[8:9], s[0:1]
	s_mov_b32 s4, 0xf800000
	v_mul_f32_e32 v7, 0x4f800000, v9
	v_cmp_gt_f32_e32 vcc, s4, v9
	s_nop 1
	v_cndmask_b32_e32 v7, v9, v7, vcc
	v_sqrt_f32_e32 v10, v7
	s_nop 0
	v_add_u32_e32 v11, -1, v10
	v_fma_f32 v12, -v11, v10, v7
	v_cmp_ge_f32_e64 s[0:1], 0, v12
	v_add_u32_e32 v12, 1, v10
	s_nop 0
	v_cndmask_b32_e64 v11, v10, v11, s[0:1]
	v_fma_f32 v10, -v12, v10, v7
	v_cmp_lt_f32_e64 s[0:1], 0, v10
	s_nop 1
	v_cndmask_b32_e64 v10, v11, v12, s[0:1]
	v_mul_f32_e32 v11, 0x37800000, v10
	v_cndmask_b32_e32 v10, v10, v11, vcc
	v_mul_f32_e32 v11, 0x4f800000, v8
	v_cmp_gt_f32_e32 vcc, s4, v8
	v_cmp_class_f32_e64 s[0:1], v7, v13
	s_nop 0
	v_cndmask_b32_e32 v11, v8, v11, vcc
	v_sqrt_f32_e32 v12, v11
	v_cndmask_b32_e64 v7, v10, v7, s[0:1]
	v_add_u32_e32 v10, -1, v12
	v_fma_f32 v15, -v10, v12, v11
	v_cmp_ge_f32_e64 s[0:1], 0, v15
	v_add_u32_e32 v15, 1, v12
	s_nop 0
	v_cndmask_b32_e64 v10, v12, v10, s[0:1]
	v_fma_f32 v12, -v15, v12, v11
	v_cmp_lt_f32_e64 s[0:1], 0, v12
	s_nop 1
	v_cndmask_b32_e64 v10, v10, v15, s[0:1]
	v_mul_f32_e32 v12, 0x37800000, v10
	v_cndmask_b32_e32 v10, v10, v12, vcc
	v_cmp_class_f32_e32 vcc, v11, v13
	s_mov_b32 s0, 0x380637bd
	s_mov_b32 s1, 0x350637bd
	v_cndmask_b32_e32 v10, v10, v11, vcc
	v_mul_f32_e32 v7, v7, v10
	v_mul_f32_e32 v7, 0x3f800347, v7
	v_pk_mul_f32 v[8:9], v[8:9], s[0:1]
	s_nop 0
	v_fmamk_f32 v7, v7, 0x3888509c, v9
	v_add_f32_e32 v7, v8, v7
	v_add_f32_e32 v7, 0xda24260, v7
	v_add_f32_e32 v6, v6, v7
	v_cmp_le_f32_e64 s[8:9], v2, v6
	v_cmp_le_f32_e64 s[6:7], v3, v6
	v_cmp_le_f32_e64 s[4:5], v4, v6
	v_lshl_add_u64 v[2:3], s[22:23], 0, v[18:19]
	s_and_b32 s19, s8, 0xffff
	s_lshl_b32 s22, s6, 16
	v_cmp_le_f32_e64 s[0:1], v5, v6
	s_or_b32 s24, s19, s22
	s_and_b32 s23, s4, 0xffff
	s_mov_b32 s22, s25
	s_or_b64 s[22:23], s[24:25], s[22:23]
	s_lshl_b32 s27, s0, 16
	s_or_b64 s[26:27], s[22:23], s[26:27]
	s_add_u32 s22, s26, -1
	s_addc_u32 s23, s27, -1
	s_and_b64 s[22:23], s[26:27], s[22:23]
	s_cmp_eq_u64 s[22:23], 0
	v_readlane_b32 s22, v14, 0
	s_cbranch_scc1 .LBB0_139
	s_mov_b64 s[92:93], s[26:27]
.Lwarm0:
	s_ff1_i32_b64 s94, s[92:93]
	s_bitset0_b64 s[92:93], s94
	s_lshl_b32 s94, s94, 10
	s_mov_b32 s95, 0
	v_lshl_add_u64 v[92:93], v[2:3], 0, s[94:95]
	global_load_dwordx4 v[88:91], v[92:93], off
	s_cmp_lg_u64 s[92:93], 0
	s_cbranch_scc1 .Lwarm0
	s_lshl_b32 s19, s29, 2
	s_add_i32 s19, s19, 0x11100
	v_mov_b32_e32 v4, s19
	ds_read_b32 v4, v4
	s_mul_i32 s19, s17, 0x2040
	v_add_u32_e32 v8, s19, v135
	v_mov_b32_e32 v15, 0x7f800000
	s_waitcnt lgkmcnt(0)
	v_max_i32_e32 v4, 1, v4
	v_cvt_f64_u32_e32 v[12:13], v4
	v_div_scale_f64 v[16:17], s[30:31], v[12:13], v[12:13], 1.0
	v_rcp_f64_e32 v[20:21], v[16:17]
	v_div_scale_f64 v[22:23], vcc, 1.0, v[12:13], 1.0
	ds_read2st64_b64 v[4:7], v8 offset0:64 offset1:65
	ds_read2st64_b64 v[8:11], v8 offset0:66 offset1:67
	v_fma_f64 v[24:25], -v[16:17], v[20:21], 1.0
	v_fmac_f64_e32 v[20:21], v[20:21], v[24:25]
	v_fma_f64 v[24:25], -v[16:17], v[20:21], 1.0
	v_fmac_f64_e32 v[20:21], v[20:21], v[24:25]
	v_mul_f64 v[24:25], v[22:23], v[20:21]
	v_fma_f64 v[16:17], -v[16:17], v[24:25], v[22:23]
	v_div_fmas_f64 v[16:17], v[16:17], v[20:21], v[24:25]
	v_div_fixup_f64 v[12:13], v[16:17], v[12:13], 1.0
	s_waitcnt lgkmcnt(1)
	v_mul_f64 v[6:7], v[6:7], v[12:13]
	v_mul_f64 v[4:5], v[4:5], v[12:13]
	s_waitcnt lgkmcnt(0)
	v_mul_f64 v[8:9], v[8:9], v[12:13]
	v_mul_f64 v[10:11], v[12:13], v[10:11]
	v_mul_f64 v[12:13], v[6:7], v[6:7]
	v_fmac_f64_e32 v[12:13], v[4:5], v[4:5]
	v_fmac_f64_e32 v[12:13], v[8:9], v[8:9]
	v_fmac_f64_e32 v[12:13], v[10:11], v[10:11]
	s_nop 1
	v_mov_b32_dpp v16, v12 quad_perm:[1,0,3,2] row_mask:0xf bank_mask:0xf bound_ctrl:1
	v_mov_b32_dpp v17, v13 quad_perm:[1,0,3,2] row_mask:0xf bank_mask:0xf bound_ctrl:1
	v_add_f64 v[12:13], v[12:13], v[16:17]
	s_nop 1
	v_mov_b32_dpp v16, v12 quad_perm:[2,3,0,1] row_mask:0xf bank_mask:0xf bound_ctrl:1
	v_mov_b32_dpp v17, v13 quad_perm:[2,3,0,1] row_mask:0xf bank_mask:0xf bound_ctrl:1
	v_add_f64 v[12:13], v[12:13], v[16:17]
	s_nop 1
	v_mov_b32_dpp v16, v12 row_half_mirror row_mask:0xf bank_mask:0xf bound_ctrl:1
	v_mov_b32_dpp v17, v13 row_half_mirror row_mask:0xf bank_mask:0xf bound_ctrl:1
	v_add_f64 v[12:13], v[12:13], v[16:17]
	s_nop 1
	v_mov_b32_dpp v16, v12 row_mirror row_mask:0xf bank_mask:0xf bound_ctrl:1
	v_mov_b32_dpp v17, v13 row_mirror row_mask:0xf bank_mask:0xf bound_ctrl:1
	v_add_f64 v[12:13], v[12:13], v[16:17]
	s_nop 0
	v_readlane_b32 s19, v13, 16
	v_readlane_b32 s23, v12, 16
	v_readlane_b32 s31, v13, 0
	v_readlane_b32 s30, v12, 0
	v_mov_b32_e32 v16, s23
	v_mov_b32_e32 v17, s19
	v_readlane_b32 s19, v13, 48
	v_readlane_b32 s23, v12, 48
	v_add_f64 v[16:17], s[30:31], v[16:17]
	v_readlane_b32 s31, v13, 32
	v_readlane_b32 s30, v12, 32
	v_mov_b32_e32 v12, s23
	v_mov_b32_e32 v13, s19
	v_add_f64 v[12:13], s[30:31], v[12:13]
	v_add_f64 v[12:13], v[16:17], v[12:13]

.LBB0_139:
	s_lshr_b32 s8, s8, 16
	s_and_b32 s19, s6, 0xffff0000
	s_mov_b32 s25, 0
	s_lshl_b64 s[26:27], s[4:5], 16
	s_or_b32 s24, s19, s8
	s_and_b32 s27, s27, 0xffff
	s_mov_b32 s26, s25
	s_or_b64 s[26:27], s[24:25], s[26:27]
	s_and_b32 s31, s0, 0xffff0000
	s_mov_b32 s30, s25
	s_or_b64 s[26:27], s[26:27], s[30:31]
	s_add_u32 s30, s26, -1
	s_addc_u32 s31, s27, -1
	s_and_b64 s[30:31], s[26:27], s[30:31]
	s_cmp_eq_u64 s[30:31], 0
	v_readlane_b32 s8, v14, 16
	s_cbranch_scc1 .LBB0_142
	s_mov_b64 s[92:93], s[26:27]
.Lwarm1:
	s_ff1_i32_b64 s94, s[92:93]
	s_bitset0_b64 s[92:93], s94
	s_lshl_b32 s94, s94, 10
	s_mov_b32 s95, 0
	v_lshl_add_u64 v[92:93], v[2:3], 0, s[94:95]
	global_load_dwordx4 v[88:91], v[92:93], off
	s_cmp_lg_u64 s[92:93], 0
	s_cbranch_scc1 .Lwarm1
	s_or_b32 s19, s29, 1
	s_lshl_b32 s23, s19, 2
	s_add_i32 s23, s23, 0x11100
	v_mov_b32_e32 v4, s23
	ds_read_b32 v4, v4
	s_mulk_i32 s19, 0x810
	v_add_u32_e32 v8, s19, v135
	v_mov_b32_e32 v15, 0x7f800000
	s_waitcnt lgkmcnt(0)
	v_max_i32_e32 v4, 1, v4
	v_cvt_f64_u32_e32 v[12:13], v4
	v_div_scale_f64 v[16:17], s[30:31], v[12:13], v[12:13], 1.0
	v_rcp_f64_e32 v[20:21], v[16:17]
	v_div_scale_f64 v[22:23], vcc, 1.0, v[12:13], 1.0
	ds_read2st64_b64 v[4:7], v8 offset0:64 offset1:65
	ds_read2st64_b64 v[8:11], v8 offset0:66 offset1:67
	v_fma_f64 v[24:25], -v[16:17], v[20:21], 1.0
	v_fmac_f64_e32 v[20:21], v[20:21], v[24:25]
	v_fma_f64 v[24:25], -v[16:17], v[20:21], 1.0
	v_fmac_f64_e32 v[20:21], v[20:21], v[24:25]
	v_mul_f64 v[24:25], v[22:23], v[20:21]
	v_fma_f64 v[16:17], -v[16:17], v[24:25], v[22:23]
	v_div_fmas_f64 v[16:17], v[16:17], v[20:21], v[24:25]
	v_div_fixup_f64 v[12:13], v[16:17], v[12:13], 1.0
	s_waitcnt lgkmcnt(1)
	v_mul_f64 v[6:7], v[6:7], v[12:13]
	v_mul_f64 v[4:5], v[4:5], v[12:13]
	s_waitcnt lgkmcnt(0)
	v_mul_f64 v[8:9], v[8:9], v[12:13]
	v_mul_f64 v[10:11], v[12:13], v[10:11]
	v_mul_f64 v[12:13], v[6:7], v[6:7]
	v_fmac_f64_e32 v[12:13], v[4:5], v[4:5]
	v_fmac_f64_e32 v[12:13], v[8:9], v[8:9]
	v_fmac_f64_e32 v[12:13], v[10:11], v[10:11]
	s_nop 1
	v_mov_b32_dpp v16, v12 quad_perm:[1,0,3,2] row_mask:0xf bank_mask:0xf bound_ctrl:1
	v_mov_b32_dpp v17, v13 quad_perm:[1,0,3,2] row_mask:0xf bank_mask:0xf bound_ctrl:1
	v_add_f64 v[12:13], v[12:13], v[16:17]
	s_nop 1
	v_mov_b32_dpp v16, v12 quad_perm:[2,3,0,1] row_mask:0xf bank_mask:0xf bound_ctrl:1
	v_mov_b32_dpp v17, v13 quad_perm:[2,3,0,1] row_mask:0xf bank_mask:0xf bound_ctrl:1
	v_add_f64 v[12:13], v[12:13], v[16:17]
	s_nop 1
	v_mov_b32_dpp v16, v12 row_half_mirror row_mask:0xf bank_mask:0xf bound_ctrl:1
	v_mov_b32_dpp v17, v13 row_half_mirror row_mask:0xf bank_mask:0xf bound_ctrl:1
	v_add_f64 v[12:13], v[12:13], v[16:17]
	s_nop 1
	v_mov_b32_dpp v16, v12 row_mirror row_mask:0xf bank_mask:0xf bound_ctrl:1
	v_mov_b32_dpp v17, v13 row_mirror row_mask:0xf bank_mask:0xf bound_ctrl:1
	v_add_f64 v[12:13], v[12:13], v[16:17]
	s_nop 0
	v_readlane_b32 s19, v13, 16
	v_readlane_b32 s23, v12, 16
	v_readlane_b32 s31, v13, 0
	v_readlane_b32 s30, v12, 0
	v_mov_b32_e32 v16, s23
	v_mov_b32_e32 v17, s19
	v_readlane_b32 s19, v13, 48
	v_readlane_b32 s23, v12, 48
	v_add_f64 v[16:17], s[30:31], v[16:17]
	v_readlane_b32 s31, v13, 32
	v_readlane_b32 s30, v12, 32
	v_mov_b32_e32 v12, s23
	v_mov_b32_e32 v13, s19
	v_add_f64 v[12:13], s[30:31], v[12:13]
	v_add_f64 v[12:13], v[16:17], v[12:13]

.LBB0_142:
	s_mov_b32 s25, 0
	s_lshr_b64 s[26:27], s[6:7], 16
	s_and_b32 s24, s9, 0xffff
	s_and_b32 s26, s26, 0xffff0000
	s_mov_b32 s27, s25
	s_or_b64 s[26:27], s[26:27], s[24:25]
	s_and_b32 s31, s5, 0xffff
	s_mov_b32 s30, s25
	s_or_b64 s[26:27], s[26:27], s[30:31]
	s_lshl_b64 s[30:31], s[0:1], 16
	s_and_b32 s31, s31, 0xffff0000
	s_mov_b32 s30, s25
	s_or_b64 s[26:27], s[26:27], s[30:31]
	s_add_u32 s30, s26, -1
	s_addc_u32 s31, s27, -1
	s_and_b64 s[30:31], s[26:27], s[30:31]
	s_cmp_eq_u64 s[30:31], 0
	v_readlane_b32 s0, v14, 32
	s_cbranch_scc1 .LBB0_145
	s_mov_b64 s[92:93], s[26:27]
.Lwarm2:
	s_ff1_i32_b64 s94, s[92:93]
	s_bitset0_b64 s[92:93], s94
	s_lshl_b32 s94, s94, 10
	s_mov_b32 s95, 0
	v_lshl_add_u64 v[92:93], v[2:3], 0, s[94:95]
	global_load_dwordx4 v[88:91], v[92:93], off
	s_cmp_lg_u64 s[92:93], 0
	s_cbranch_scc1 .Lwarm2
	s_or_b32 s6, s29, 2
	s_lshl_b32 s19, s6, 2
	s_add_i32 s19, s19, 0x11100
	v_mov_b32_e32 v4, s19
	ds_read_b32 v4, v4
	s_mulk_i32 s6, 0x810
	v_add_u32_e32 v8, s6, v135
	v_mov_b32_e32 v15, 0x7f800000
	s_waitcnt lgkmcnt(0)
	v_max_i32_e32 v4, 1, v4
	v_cvt_f64_u32_e32 v[12:13], v4
	v_div_scale_f64 v[16:17], s[30:31], v[12:13], v[12:13], 1.0
	v_rcp_f64_e32 v[20:21], v[16:17]
	v_div_scale_f64 v[22:23], vcc, 1.0, v[12:13], 1.0
	ds_read2st64_b64 v[4:7], v8 offset0:64 offset1:65
	ds_read2st64_b64 v[8:11], v8 offset0:66 offset1:67
	v_fma_f64 v[24:25], -v[16:17], v[20:21], 1.0
	v_fmac_f64_e32 v[20:21], v[20:21], v[24:25]
	v_fma_f64 v[24:25], -v[16:17], v[20:21], 1.0
	v_fmac_f64_e32 v[20:21], v[20:21], v[24:25]
	v_mul_f64 v[24:25], v[22:23], v[20:21]
	v_fma_f64 v[16:17], -v[16:17], v[24:25], v[22:23]
	v_div_fmas_f64 v[16:17], v[16:17], v[20:21], v[24:25]
	v_div_fixup_f64 v[12:13], v[16:17], v[12:13], 1.0
	s_waitcnt lgkmcnt(1)
	v_mul_f64 v[6:7], v[6:7], v[12:13]
	v_mul_f64 v[4:5], v[4:5], v[12:13]
	s_waitcnt lgkmcnt(0)
	v_mul_f64 v[8:9], v[8:9], v[12:13]
	v_mul_f64 v[10:11], v[12:13], v[10:11]
	v_mul_f64 v[12:13], v[6:7], v[6:7]
	v_fmac_f64_e32 v[12:13], v[4:5], v[4:5]
	v_fmac_f64_e32 v[12:13], v[8:9], v[8:9]
	v_fmac_f64_e32 v[12:13], v[10:11], v[10:11]
	s_nop 1
	v_mov_b32_dpp v16, v12 quad_perm:[1,0,3,2] row_mask:0xf bank_mask:0xf bound_ctrl:1
	v_mov_b32_dpp v17, v13 quad_perm:[1,0,3,2] row_mask:0xf bank_mask:0xf bound_ctrl:1
	v_add_f64 v[12:13], v[12:13], v[16:17]
	s_nop 1
	v_mov_b32_dpp v16, v12 quad_perm:[2,3,0,1] row_mask:0xf bank_mask:0xf bound_ctrl:1
	v_mov_b32_dpp v17, v13 quad_perm:[2,3,0,1] row_mask:0xf bank_mask:0xf bound_ctrl:1
	v_add_f64 v[12:13], v[12:13], v[16:17]
	s_nop 1
	v_mov_b32_dpp v16, v12 row_half_mirror row_mask:0xf bank_mask:0xf bound_ctrl:1
	v_mov_b32_dpp v17, v13 row_half_mirror row_mask:0xf bank_mask:0xf bound_ctrl:1
	v_add_f64 v[12:13], v[12:13], v[16:17]
	s_nop 1
	v_mov_b32_dpp v16, v12 row_mirror row_mask:0xf bank_mask:0xf bound_ctrl:1
	v_mov_b32_dpp v17, v13 row_mirror row_mask:0xf bank_mask:0xf bound_ctrl:1
	v_add_f64 v[12:13], v[12:13], v[16:17]
	s_nop 0
	v_readlane_b32 s6, v13, 16
	v_readlane_b32 s19, v12, 16
	v_readlane_b32 s31, v13, 0
	v_readlane_b32 s30, v12, 0
	v_mov_b32_e32 v16, s19
	v_mov_b32_e32 v17, s6
	v_readlane_b32 s6, v13, 48
	v_readlane_b32 s19, v12, 48
	v_add_f64 v[16:17], s[30:31], v[16:17]
	v_readlane_b32 s31, v13, 32
	v_readlane_b32 s30, v12, 32
	v_mov_b32_e32 v12, s19
	v_mov_b32_e32 v13, s6
	v_add_f64 v[12:13], s[30:31], v[12:13]
	v_add_f64 v[12:13], v[16:17], v[12:13]

.LBB0_145:
	s_mov_b32 s25, 0
	s_lshr_b32 s24, s9, 16
	s_and_b32 s6, s7, 0xffff0000
	s_mov_b32 s7, s25
	s_lshr_b64 s[4:5], s[4:5], 16
	s_or_b64 s[6:7], s[6:7], s[24:25]
	s_mov_b32 s4, s25
	s_or_b64 s[4:5], s[6:7], s[4:5]
	s_and_b32 s7, s1, 0xffff0000
	s_mov_b32 s6, s25
	s_or_b64 s[6:7], s[4:5], s[6:7]
	s_add_u32 s4, s6, -1
	s_addc_u32 s5, s7, -1
	s_and_b64 s[4:5], s[6:7], s[4:5]
	s_cmp_eq_u64 s[4:5], 0
	v_readlane_b32 s4, v14, 48
	s_cbranch_scc1 .LBB0_148
	s_mov_b64 s[92:93], s[6:7]
.Lwarm3:
	s_ff1_i32_b64 s94, s[92:93]
	s_bitset0_b64 s[92:93], s94
	s_lshl_b32 s94, s94, 10
	s_mov_b32 s95, 0
	v_lshl_add_u64 v[92:93], v[2:3], 0, s[94:95]
	global_load_dwordx4 v[88:91], v[92:93], off
	s_cmp_lg_u64 s[92:93], 0
	s_cbranch_scc1 .Lwarm3
	s_or_b32 s1, s29, 3
	s_lshl_b32 s5, s1, 2
	s_add_i32 s5, s5, 0x11100
	v_mov_b32_e32 v4, s5
	ds_read_b32 v4, v4
	s_mulk_i32 s1, 0x810
	v_add_u32_e32 v8, s1, v135
	s_waitcnt lgkmcnt(0)
	v_max_i32_e32 v4, 1, v4
	v_cvt_f64_u32_e32 v[12:13], v4
	v_div_scale_f64 v[14:15], s[26:27], v[12:13], v[12:13], 1.0
	v_rcp_f64_e32 v[16:17], v[14:15]
	v_div_scale_f64 v[20:21], vcc, 1.0, v[12:13], 1.0
	ds_read2st64_b64 v[4:7], v8 offset0:64 offset1:65
	ds_read2st64_b64 v[8:11], v8 offset0:66 offset1:67
	v_fma_f64 v[22:23], -v[14:15], v[16:17], 1.0
	v_fmac_f64_e32 v[16:17], v[16:17], v[22:23]
	v_fma_f64 v[22:23], -v[14:15], v[16:17], 1.0
	v_fmac_f64_e32 v[16:17], v[16:17], v[22:23]
	v_mul_f64 v[22:23], v[20:21], v[16:17]
	v_fma_f64 v[14:15], -v[14:15], v[22:23], v[20:21]
	v_div_fmas_f64 v[14:15], v[14:15], v[16:17], v[22:23]
	v_div_fixup_f64 v[12:13], v[14:15], v[12:13], 1.0
	s_waitcnt lgkmcnt(1)
	v_mul_f64 v[6:7], v[6:7], v[12:13]
	v_mul_f64 v[4:5], v[4:5], v[12:13]
	s_waitcnt lgkmcnt(0)
	v_mul_f64 v[8:9], v[8:9], v[12:13]
	v_mul_f64 v[10:11], v[12:13], v[10:11]
	v_mul_f64 v[12:13], v[6:7], v[6:7]
	v_fmac_f64_e32 v[12:13], v[4:5], v[4:5]
	v_fmac_f64_e32 v[12:13], v[8:9], v[8:9]
	v_fmac_f64_e32 v[12:13], v[10:11], v[10:11]
	s_nop 1
	v_mov_b32_dpp v14, v12 quad_perm:[1,0,3,2] row_mask:0xf bank_mask:0xf bound_ctrl:1
	v_mov_b32_dpp v15, v13 quad_perm:[1,0,3,2] row_mask:0xf bank_mask:0xf bound_ctrl:1
	v_add_f64 v[12:13], v[12:13], v[14:15]
	s_nop 1
	v_mov_b32_dpp v14, v12 quad_perm:[2,3,0,1] row_mask:0xf bank_mask:0xf bound_ctrl:1
	v_mov_b32_dpp v15, v13 quad_perm:[2,3,0,1] row_mask:0xf bank_mask:0xf bound_ctrl:1
	v_add_f64 v[12:13], v[12:13], v[14:15]
	s_nop 1
	v_mov_b32_dpp v14, v12 row_half_mirror row_mask:0xf bank_mask:0xf bound_ctrl:1
	v_mov_b32_dpp v15, v13 row_half_mirror row_mask:0xf bank_mask:0xf bound_ctrl:1
	v_add_f64 v[12:13], v[12:13], v[14:15]
	s_nop 1
	v_mov_b32_dpp v14, v12 row_mirror row_mask:0xf bank_mask:0xf bound_ctrl:1
	v_mov_b32_dpp v15, v13 row_mirror row_mask:0xf bank_mask:0xf bound_ctrl:1
	v_add_f64 v[12:13], v[12:13], v[14:15]
	s_nop 0
	v_readlane_b32 s1, v13, 16
	v_readlane_b32 s5, v12, 16
	v_readlane_b32 s27, v13, 0
	v_readlane_b32 s26, v12, 0
	v_mov_b32_e32 v14, s5
	v_mov_b32_e32 v15, s1
	v_readlane_b32 s1, v13, 48
	v_readlane_b32 s5, v12, 48
	v_add_f64 v[14:15], s[26:27], v[14:15]
	v_readlane_b32 s27, v13, 32
	v_readlane_b32 s26, v12, 32
	v_mov_b32_e32 v12, s5
	v_mov_b32_e32 v13, s1
	v_add_f64 v[12:13], s[26:27], v[12:13]
	v_add_f64 v[12:13], v[14:15], v[12:13]
	v_mov_b32_e32 v14, 0x7f800000
